# k_gcn: MLP tail-input loads (x[:,0:2], xtemp) hoisted from before the block barrier to the prologue
# speedup vs baseline: 1.0145x; 1.0019x over previous
_Z5k_gcnILi128ELb1ELi16EEvPKDv8_DF16_PKiS4_PKfS2_S6_PDF16_S6_S6_S2_S6_S2_S6_S6_S6_PfS4_:
	s_load_dwordx4 s[20:23], s[0:1], 0x8
	s_load_dwordx2 s[4:5], s[0:1], 0x20
	v_readfirstlane_b32 s30, v0
	v_and_b32_e32 v1, 63, v0
	s_lshr_b32 s28, s30, 6
	v_lshl_or_b32 v2, s28, 9, v1
	v_mov_b32_e32 v3, 0
	v_bfe_u32 v83, v0, 4, 2
	s_waitcnt lgkmcnt(0)
	v_lshl_add_u64 v[14:15], v[2:3], 4, s[4:5]
	v_ashrrev_i32_e32 v3, 31, v2
	s_lshl_b32 s29, s2, 4
	s_lshl_b32 s6, s28, 2
	v_or_b32_e32 v38, s29, v83
	v_add_lshl_u32 v38, v38, s6, 2
	global_load_dwordx2 v[50:51], v38, s[20:21]
	v_lshl_add_u64 v[16:17], v[2:3], 4, s[4:5]
	global_load_dwordx4 v[26:29], v[14:15], off
	global_load_dwordx4 v[10:13], v[16:17], off offset:1024
	global_load_dwordx4 v[6:9], v[16:17], off offset:2048
	global_load_dwordx4 v[2:5], v[16:17], off offset:3072
	v_or_b32_e32 v14, s29, v83
	s_lshl_b32 s6, s28, 2
	v_add_u32_e32 v14, s6, v14
	s_movk_i32 s3, 0x1000
	v_ashrrev_i32_e32 v15, 31, v14
	v_add_co_u32_e32 v34, vcc, s3, v16
	v_lshl_add_u64 v[36:37], v[14:15], 2, s[20:21]
	s_nop 0
	v_addc_co_u32_e32 v35, vcc, 0, v17, vcc
	global_load_dwordx4 v[30:33], v[34:35], off
	global_load_dwordx4 v[22:25], v[34:35], off offset:1024
	global_load_dwordx4 v[18:21], v[34:35], off offset:2048
	global_load_dwordx4 v[14:17], v[34:35], off offset:3072
	s_waitcnt vmcnt(8)
	v_sub_u32_e32 v53, v51, v50
	v_lshlrev_b32_e32 v34, 2, v50
	global_load_dword v36, v34, s[22:23]
	global_load_dword v38, v34, s[22:23] offset:4
	global_load_dword v42, v34, s[22:23] offset:8
	global_load_dword v46, v34, s[22:23] offset:12
	s_load_dwordx2 s[24:25], s[0:1], 0x0
	s_load_dwordx2 s[2:3], s[0:1], 0x18
	v_and_b32_e32 v82, 15, v0
	v_or_b32_e32 v51, s6, v83
	v_add_u32_e32 v34, s29, v51
	v_lshlrev_b32_e32 v54, 4, v82
	s_mov_b32 s27, 0x20000
	s_mov_b32 s26, 0x4e2100
	s_waitcnt lgkmcnt(0)
	s_and_b32 s25, s25, 0xffff
	v_lshl_or_b32 v35, v34, 8, v54
	buffer_load_dwordx4 v[64:67], v35, s[24:27], 0 offen
	v_ashrrev_i32_e32 v35, 31, v34
	v_lshl_add_u64 v[34:35], v[34:35], 2, s[2:3]
	global_load_dword v52, v[34:35], off
	v_mbcnt_lo_u32_b32 v34, -1, 0
	v_mbcnt_hi_u32_b32 v34, -1, v34
	v_and_b32_e32 v37, 64, v34
	v_xor_b32_e32 v35, 32, v34
	v_add_u32_e32 v37, 64, v37
	v_cmp_lt_i32_e32 vcc, v35, v37
	v_xor_b32_e32 v39, 16, v34
	s_load_dwordx2 s[2:3], s[0:1], 0x78
	s_load_dwordx8 s[4:11], s[0:1], 0x58
	s_load_dwordx8 s[12:19], s[0:1], 0x38
	v_cndmask_b32_e32 v35, v34, v35, vcc
	v_lshlrev_b32_e32 v84, 2, v35
	ds_bpermute_b32 v35, v84, v53
	v_cmp_lt_i32_e32 vcc, v39, v37
	s_mov_b32 s33, 4
	s_waitcnt vmcnt(1)
	v_mov_b32_e32 v70, 0x4e20
	v_cmp_lt_i32_e64 s[34:35], 0, v53
	v_cmp_lt_i32_e64 s[36:37], 1, v53
	v_cmp_lt_i32_e64 s[38:39], 2, v53
	v_cmp_lt_i32_e64 s[40:41], 3, v53
	v_cndmask_b32_e64 v36, v70, v36, s[34:35]
	v_cndmask_b32_e64 v38, v70, v38, s[36:37]
	v_cndmask_b32_e64 v42, v70, v42, s[38:39]
	v_cndmask_b32_e64 v46, v70, v46, s[40:41]
	v_cvt_f32_f16_e32 v62, v64
	v_cndmask_b32_e32 v34, v34, v39, vcc
	v_lshlrev_b32_e32 v85, 2, v34
	s_waitcnt lgkmcnt(0)
	v_cmp_gt_u32_e64 s[36:37], 16, v0
	s_and_saveexec_b64 s[38:39], s[36:37]
	s_cbranch_execz .Lkg_tail_skip
	v_or_b32_e32 v80, s29, v0
	v_mul_u32_u24_e32 v81, 0x108, v80
	v_lshlrev_b32_e32 v94, 2, v80
	global_load_dwordx2 v[80:81], v81, s[12:13]
	global_load_dword v94, v94, s[14:15]
.Lkg_tail_skip:
	s_mov_b64 exec, s[38:39]
	v_max_i32_e32 v34, v53, v35
	ds_bpermute_b32 v35, v85, v34
	v_cvt_f32_f16_sdwa v63, v64 dst_sel:DWORD dst_unused:UNUSED_PAD src0_sel:WORD_1
	v_cvt_f32_f16_e32 v60, v65
	v_cvt_f32_f16_sdwa v61, v65 dst_sel:DWORD dst_unused:UNUSED_PAD src0_sel:WORD_1
	v_cvt_f32_f16_e32 v58, v66
	v_cvt_f32_f16_sdwa v59, v66 dst_sel:DWORD dst_unused:UNUSED_PAD src0_sel:WORD_1
	v_cvt_f32_f16_e32 v56, v67
	v_cvt_f32_f16_sdwa v57, v67 dst_sel:DWORD dst_unused:UNUSED_PAD src0_sel:WORD_1
	s_waitcnt lgkmcnt(0)
	v_max_i32_e32 v34, v34, v35
	s_nop 0
	v_readfirstlane_b32 s31, v34
	s_cmp_lt_i32 s31, 1
	s_cbranch_scc1 .LBB2_19

.LBB2_19:
	s_load_dwordx2 s[0:1], s[0:1], 0x28
	v_mov_b32_e32 v35, 0
	v_lshlrev_b32_e32 v34, 4, v83
	s_lshl_b32 s20, s28, 5
	s_mov_b32 s21, 0
	s_waitcnt lgkmcnt(0)
	v_lshl_add_u64 v[36:37], s[0:1], 0, v[34:35]
	v_lshl_add_u64 v[36:37], s[20:21], 2, v[36:37]
	global_load_dwordx4 v[70:73], v[36:37], off
	global_load_dwordx4 v[74:77], v[36:37], off offset:64
	v_mov_b32_e32 v36, v63
	v_mov_b32_e32 v37, v60
	s_waitcnt vmcnt(2)
	v_pk_mul_f32 v[36:37], v[52:53], v[36:37] op_sel_hi:[0,1]
	v_mov_b32_e32 v38, v61
	v_mov_b32_e32 v39, v58
	v_fma_mixlo_f16 v34, v52, v62, 0
	v_cvt_pk_f16_f32 v37, v36, v37
	v_pk_mul_f32 v[38:39], v[52:53], v[38:39] op_sel_hi:[0,1]
	v_pack_b32_f16 v36, v34, v37
	v_cvt_pk_f16_f32 v34, v38, v39
	v_mov_b32_e32 v38, v59
	v_mov_b32_e32 v39, v56
	v_pk_mul_f32 v[38:39], v[52:53], v[38:39] op_sel_hi:[0,1]
	v_cvt_pk_f16_f32 v39, v38, v39
	s_movk_i32 s20, 0x110
	v_alignbit_b32 v38, v39, v34, 16
	v_lshrrev_b32_e32 v39, 16, v39
	v_mad_u64_u32 v[40:41], s[0:1], v51, s20, v[54:55]
	v_alignbit_b32 v37, v34, v37, 16
	v_fma_mixhi_f16 v39, v52, v57, 0
	v_lshlrev_b32_e32 v86, 2, v83
	v_cmp_gt_u32_e32 vcc, 16, v0
	v_mov_b32_e32 v87, 0
	v_mov_b32_e32 v88, 0
	v_mov_b32_e32 v89, 0
	ds_write_b128 v40, v[36:39] offset:5376
	s_and_saveexec_b64 s[0:1], vcc
	s_cbranch_execz .LBB2_21
	s_waitcnt vmcnt(2)
	v_max_f32_e32 v36, 0, v80
	v_max_f32_e32 v37, 0, v81
	v_max_f32_e32 v34, 0, v94
	v_cvt_f16_f32_e32 v88, v36
	v_cvt_f16_f32_e32 v87, v34
	v_cvt_f16_f32_e32 v89, v37
